# bf16 GEMMs (P8,P19): 8-row x 128-B LDS subtile image (full-line LDS-DMA) on top of the scalar-base DMA form
# speedup vs baseline: 1.0007x; 1.0007x over previous
.LBB0_620:
	ds_read_b128 v[152:155], v148
	ds_read_b128 v[156:159], v230
	ds_read_b128 v[160:163], v148 offset:2048
	ds_read_b128 v[164:167], v230 offset:2048
	s_add_u32 s30, s28, 0xfff80080
	s_addc_u32 s31, s29, -1
	s_cmp_eq_u32 s60, 28
	s_cselect_b32 s35, s21, s31
	s_cselect_b32 s34, s54, s30
	s_cselect_b32 s31, s19, s57
	s_cselect_b32 s30, s55, s56
	s_add_i32 m0, s17, 0xc000
	ds_read_b128 v[168:171], v149
	ds_read_b128 v[172:175], v229
	ds_read_b128 v[176:179], v149 offset:2048
	ds_read_b128 v[180:183], v229 offset:2048
	ds_read_b128 v[184:187], v149 offset:4096
	ds_read_b128 v[188:191], v229 offset:4096
	ds_read_b128 v[192:195], v149 offset:6144
	ds_read_b128 v[196:199], v229 offset:6144
	global_load_lds_dwordx4 v138, s[28:29]
	s_add_i32 m0, s17, 0xe000
	s_nop 0
	global_load_lds_dwordx4 v140, s[28:29]
	s_waitcnt lgkmcnt(8)
	s_barrier
	s_waitcnt lgkmcnt(0)
	s_setprio 1
	s_waitcnt lgkmcnt(0)
	v_mfma_f32_16x16x32_bf16 v[126:129], v[152:155], v[168:171], v[126:129]
	v_mfma_f32_16x16x32_bf16 v[122:125], v[160:163], v[168:171], v[122:125]
	v_mfma_f32_16x16x32_bf16 v[118:121], v[152:155], v[176:179], v[118:121]
	v_mfma_f32_16x16x32_bf16 v[114:117], v[160:163], v[176:179], v[114:117]
	v_mfma_f32_16x16x32_bf16 v[102:105], v[152:155], v[184:187], v[102:105]
	v_mfma_f32_16x16x32_bf16 v[98:101], v[160:163], v[184:187], v[98:101]
	v_mfma_f32_16x16x32_bf16 v[86:89], v[152:155], v[192:195], v[86:89]
	v_mfma_f32_16x16x32_bf16 v[82:85], v[160:163], v[192:195], v[82:85]
	v_mfma_f32_16x16x32_bf16 v[126:129], v[156:159], v[172:175], v[126:129]
	v_mfma_f32_16x16x32_bf16 v[122:125], v[164:167], v[172:175], v[122:125]
	v_mfma_f32_16x16x32_bf16 v[118:121], v[156:159], v[180:183], v[118:121]
	v_mfma_f32_16x16x32_bf16 v[114:117], v[164:167], v[180:183], v[114:117]
	v_mfma_f32_16x16x32_bf16 v[102:105], v[156:159], v[188:191], v[102:105]
	v_mfma_f32_16x16x32_bf16 v[98:101], v[164:167], v[188:191], v[98:101]
	v_mfma_f32_16x16x32_bf16 v[86:89], v[156:159], v[196:199], v[86:89]
	v_mfma_f32_16x16x32_bf16 v[82:85], v[164:167], v[196:199], v[82:85]
	s_setprio 0
	s_barrier
	s_add_i32 s61, s47, s37
	s_add_u32 s66, s30, 0x80
	s_addc_u32 s67, s31, 0
	s_mov_b32 m0, s61
	ds_read_b128 v[200:203], v150
	ds_read_b128 v[206:209], v231
	ds_read_b128 v[210:213], v150 offset:2048
	ds_read_b128 v[214:217], v231 offset:2048
	global_load_lds_dwordx4 v134, s[30:31]
	s_add_i32 m0, s61, 0x2000
	s_nop 0
	global_load_lds_dwordx4 v130, s[30:31]
	s_barrier
	s_waitcnt lgkmcnt(0)
	s_setprio 1
	s_waitcnt lgkmcnt(0)
	v_mfma_f32_16x16x32_bf16 v[110:113], v[200:203], v[168:171], v[110:113]
	v_mfma_f32_16x16x32_bf16 v[106:109], v[210:213], v[168:171], v[106:109]
	v_mfma_f32_16x16x32_bf16 v[94:97], v[200:203], v[176:179], v[94:97]
	v_mfma_f32_16x16x32_bf16 v[90:93], v[210:213], v[176:179], v[90:93]
	v_mfma_f32_16x16x32_bf16 v[78:81], v[200:203], v[184:187], v[78:81]
	v_mfma_f32_16x16x32_bf16 v[74:77], v[210:213], v[184:187], v[74:77]
	v_mfma_f32_16x16x32_bf16 v[70:73], v[200:203], v[192:195], v[70:73]
	v_mfma_f32_16x16x32_bf16 v[66:69], v[210:213], v[192:195], v[66:69]
	v_mfma_f32_16x16x32_bf16 v[110:113], v[206:209], v[172:175], v[110:113]
	v_mfma_f32_16x16x32_bf16 v[106:109], v[214:217], v[172:175], v[106:109]
	v_mfma_f32_16x16x32_bf16 v[94:97], v[206:209], v[180:183], v[94:97]
	v_mfma_f32_16x16x32_bf16 v[90:93], v[214:217], v[180:183], v[90:93]
	v_mfma_f32_16x16x32_bf16 v[78:81], v[206:209], v[188:191], v[78:81]
	v_mfma_f32_16x16x32_bf16 v[74:77], v[214:217], v[188:191], v[74:77]
	v_mfma_f32_16x16x32_bf16 v[70:73], v[206:209], v[196:199], v[70:73]
	v_mfma_f32_16x16x32_bf16 v[66:69], v[214:217], v[196:199], v[66:69]
	s_setprio 0
	s_mov_b32 m0, s17
	s_add_u32 s68, s34, 0x80
	s_addc_u32 s69, s35, 0
	s_barrier
	ds_read_b128 v[168:171], v149 offset:16384
	ds_read_b128 v[172:175], v229 offset:16384
	ds_read_b128 v[176:179], v149 offset:18432
	ds_read_b128 v[180:183], v229 offset:18432
	ds_read_b128 v[184:187], v149 offset:20480
	ds_read_b128 v[188:191], v229 offset:20480
	ds_read_b128 v[192:195], v149 offset:22528
	ds_read_b128 v[196:199], v229 offset:22528
	global_load_lds_dwordx4 v136, s[34:35]
	s_mov_b32 m0, s40
	s_nop 0
	global_load_lds_dwordx4 v132, s[34:35]
	s_barrier
	s_waitcnt lgkmcnt(0)
	s_setprio 1
	s_waitcnt lgkmcnt(0)
	v_mfma_f32_16x16x32_bf16 v[62:65], v[152:155], v[168:171], v[62:65]
	v_mfma_f32_16x16x32_bf16 v[58:61], v[160:163], v[168:171], v[58:61]
	v_mfma_f32_16x16x32_bf16 v[54:57], v[152:155], v[176:179], v[54:57]
	v_mfma_f32_16x16x32_bf16 v[50:53], v[160:163], v[176:179], v[50:53]
	v_mfma_f32_16x16x32_bf16 v[38:41], v[152:155], v[184:187], v[38:41]
	v_mfma_f32_16x16x32_bf16 v[34:37], v[160:163], v[184:187], v[34:37]
	v_mfma_f32_16x16x32_bf16 v[22:25], v[152:155], v[192:195], v[22:25]
	v_mfma_f32_16x16x32_bf16 v[18:21], v[160:163], v[192:195], v[18:21]
	v_mfma_f32_16x16x32_bf16 v[62:65], v[156:159], v[172:175], v[62:65]
	v_mfma_f32_16x16x32_bf16 v[58:61], v[164:167], v[172:175], v[58:61]
	v_mfma_f32_16x16x32_bf16 v[54:57], v[156:159], v[180:183], v[54:57]
	v_mfma_f32_16x16x32_bf16 v[50:53], v[164:167], v[180:183], v[50:53]
	v_mfma_f32_16x16x32_bf16 v[38:41], v[156:159], v[188:191], v[38:41]
	v_mfma_f32_16x16x32_bf16 v[34:37], v[164:167], v[188:191], v[34:37]
	v_mfma_f32_16x16x32_bf16 v[22:25], v[156:159], v[196:199], v[22:25]
	v_mfma_f32_16x16x32_bf16 v[18:21], v[164:167], v[196:199], v[18:21]
	s_setprio 0
	s_barrier
	s_add_u32 s62, s30, 0x80000
	s_addc_u32 s63, s31, 0
	s_add_i32 s61, s48, s37
	s_mov_b32 m0, s61
	s_nop 0
	global_load_lds_dwordx4 v134, s[62:63]
	s_add_i32 m0, s61, 0x2000
	s_nop 0
	global_load_lds_dwordx4 v130, s[62:63]
	s_waitcnt vmcnt(6)
	s_barrier
	s_setprio 1
	v_mfma_f32_16x16x32_bf16 v[46:49], v[200:203], v[168:171], v[46:49]
	v_mfma_f32_16x16x32_bf16 v[42:45], v[210:213], v[168:171], v[42:45]
	v_mfma_f32_16x16x32_bf16 v[30:33], v[200:203], v[176:179], v[30:33]
	v_mfma_f32_16x16x32_bf16 v[26:29], v[210:213], v[176:179], v[26:29]
	v_mfma_f32_16x16x32_bf16 v[14:17], v[200:203], v[184:187], v[14:17]
	v_mfma_f32_16x16x32_bf16 v[10:13], v[210:213], v[184:187], v[10:13]
	v_mfma_f32_16x16x32_bf16 v[6:9], v[200:203], v[192:195], v[6:9]
	v_mfma_f32_16x16x32_bf16 v[2:5], v[210:213], v[192:195], v[2:5]
	v_mfma_f32_16x16x32_bf16 v[46:49], v[206:209], v[172:175], v[46:49]
	v_mfma_f32_16x16x32_bf16 v[42:45], v[214:217], v[172:175], v[42:45]
	v_mfma_f32_16x16x32_bf16 v[30:33], v[206:209], v[180:183], v[30:33]
	v_mfma_f32_16x16x32_bf16 v[26:29], v[214:217], v[180:183], v[26:29]
	v_mfma_f32_16x16x32_bf16 v[14:17], v[206:209], v[188:191], v[14:17]
	v_mfma_f32_16x16x32_bf16 v[10:13], v[214:217], v[188:191], v[10:13]
	v_mfma_f32_16x16x32_bf16 v[6:9], v[206:209], v[196:199], v[6:9]
	v_mfma_f32_16x16x32_bf16 v[2:5], v[214:217], v[196:199], v[2:5]
	s_setprio 0
	s_add_i32 s61, 0, 0x18000
	v_add_u32_e32 v151, s61, v146
	v_xor_b32_e32 v232, 64, v151
	s_barrier
	ds_read_b128 v[152:155], v151
	ds_read_b128 v[156:159], v232
	ds_read_b128 v[160:163], v151 offset:2048
	ds_read_b128 v[164:167], v232 offset:2048
	s_add_u32 s34, s34, 0x80000
	s_addc_u32 s35, s35, 0
	s_mov_b32 m0, s41
	ds_read_b128 v[168:171], v149 offset:32768
	ds_read_b128 v[172:175], v229 offset:32768
	ds_read_b128 v[176:179], v149 offset:34816
	ds_read_b128 v[180:183], v229 offset:34816
	ds_read_b128 v[184:187], v149 offset:36864
	ds_read_b128 v[188:191], v229 offset:36864
	ds_read_b128 v[192:195], v149 offset:38912
	ds_read_b128 v[196:199], v229 offset:38912
	global_load_lds_dwordx4 v136, s[34:35]
	s_mov_b32 m0, s42
	s_nop 0
	global_load_lds_dwordx4 v132, s[34:35]
	s_waitcnt lgkmcnt(8)
	s_barrier
	s_waitcnt lgkmcnt(0)
	s_setprio 1
	s_waitcnt lgkmcnt(0)
	v_mfma_f32_16x16x32_bf16 v[126:129], v[152:155], v[168:171], v[126:129]
	v_mfma_f32_16x16x32_bf16 v[122:125], v[160:163], v[168:171], v[122:125]
	v_mfma_f32_16x16x32_bf16 v[118:121], v[152:155], v[176:179], v[118:121]
	v_mfma_f32_16x16x32_bf16 v[114:117], v[160:163], v[176:179], v[114:117]
	v_mfma_f32_16x16x32_bf16 v[102:105], v[152:155], v[184:187], v[102:105]
	v_mfma_f32_16x16x32_bf16 v[98:101], v[160:163], v[184:187], v[98:101]
	v_mfma_f32_16x16x32_bf16 v[86:89], v[152:155], v[192:195], v[86:89]
	v_mfma_f32_16x16x32_bf16 v[82:85], v[160:163], v[192:195], v[82:85]
	v_mfma_f32_16x16x32_bf16 v[126:129], v[156:159], v[172:175], v[126:129]
	v_mfma_f32_16x16x32_bf16 v[122:125], v[164:167], v[172:175], v[122:125]
	v_mfma_f32_16x16x32_bf16 v[118:121], v[156:159], v[180:183], v[118:121]
	v_mfma_f32_16x16x32_bf16 v[114:117], v[164:167], v[180:183], v[114:117]
	v_mfma_f32_16x16x32_bf16 v[102:105], v[156:159], v[188:191], v[102:105]
	v_mfma_f32_16x16x32_bf16 v[98:101], v[164:167], v[188:191], v[98:101]
	v_mfma_f32_16x16x32_bf16 v[86:89], v[156:159], v[196:199], v[86:89]
	v_mfma_f32_16x16x32_bf16 v[82:85], v[164:167], v[196:199], v[82:85]
	s_setprio 0
	s_barrier
	s_add_i32 s34, 0, 0x1c000
	s_add_i32 s35, s61, s37
	v_add_u32_e32 v151, s34, v146
	v_xor_b32_e32 v232, 64, v151
	s_mov_b32 m0, s35
	ds_read_b128 v[200:203], v151
	ds_read_b128 v[206:209], v232
	ds_read_b128 v[210:213], v151 offset:2048
	ds_read_b128 v[214:217], v232 offset:2048
	global_load_lds_dwordx4 v134, s[66:67]
	s_add_i32 m0, s35, 0x2000
	s_nop 0
	global_load_lds_dwordx4 v130, s[66:67]
	s_barrier
	s_waitcnt lgkmcnt(0)
	s_setprio 1
	s_waitcnt lgkmcnt(0)
	v_mfma_f32_16x16x32_bf16 v[110:113], v[200:203], v[168:171], v[110:113]
	v_mfma_f32_16x16x32_bf16 v[106:109], v[210:213], v[168:171], v[106:109]
	v_mfma_f32_16x16x32_bf16 v[94:97], v[200:203], v[176:179], v[94:97]
	v_mfma_f32_16x16x32_bf16 v[90:93], v[210:213], v[176:179], v[90:93]
	v_mfma_f32_16x16x32_bf16 v[78:81], v[200:203], v[184:187], v[78:81]
	v_mfma_f32_16x16x32_bf16 v[74:77], v[210:213], v[184:187], v[74:77]
	v_mfma_f32_16x16x32_bf16 v[70:73], v[200:203], v[192:195], v[70:73]
	v_mfma_f32_16x16x32_bf16 v[66:69], v[210:213], v[192:195], v[66:69]
	v_mfma_f32_16x16x32_bf16 v[110:113], v[206:209], v[172:175], v[110:113]
	v_mfma_f32_16x16x32_bf16 v[106:109], v[214:217], v[172:175], v[106:109]
	v_mfma_f32_16x16x32_bf16 v[94:97], v[206:209], v[180:183], v[94:97]
	v_mfma_f32_16x16x32_bf16 v[90:93], v[214:217], v[180:183], v[90:93]
	v_mfma_f32_16x16x32_bf16 v[78:81], v[206:209], v[188:191], v[78:81]
	v_mfma_f32_16x16x32_bf16 v[74:77], v[214:217], v[188:191], v[74:77]
	v_mfma_f32_16x16x32_bf16 v[70:73], v[206:209], v[196:199], v[70:73]
	v_mfma_f32_16x16x32_bf16 v[66:69], v[214:217], v[196:199], v[66:69]
	s_setprio 0
	s_mov_b32 m0, s44
	s_barrier
	ds_read_b128 v[168:171], v149 offset:49152
	ds_read_b128 v[172:175], v229 offset:49152
	ds_read_b128 v[176:179], v149 offset:51200
	ds_read_b128 v[180:183], v229 offset:51200
	ds_read_b128 v[184:187], v149 offset:53248
	ds_read_b128 v[188:191], v229 offset:53248
	ds_read_b128 v[192:195], v149 offset:55296
	ds_read_b128 v[196:199], v229 offset:55296
	global_load_lds_dwordx4 v136, s[68:69]
	s_mov_b32 m0, s45
	s_nop 0
	global_load_lds_dwordx4 v132, s[68:69]
	s_barrier
	s_waitcnt lgkmcnt(0)
	s_setprio 1
	s_waitcnt lgkmcnt(0)
	v_mfma_f32_16x16x32_bf16 v[62:65], v[152:155], v[168:171], v[62:65]
	v_mfma_f32_16x16x32_bf16 v[58:61], v[160:163], v[168:171], v[58:61]
	v_mfma_f32_16x16x32_bf16 v[54:57], v[152:155], v[176:179], v[54:57]
	v_mfma_f32_16x16x32_bf16 v[50:53], v[160:163], v[176:179], v[50:53]
	v_mfma_f32_16x16x32_bf16 v[38:41], v[152:155], v[184:187], v[38:41]
	v_mfma_f32_16x16x32_bf16 v[34:37], v[160:163], v[184:187], v[34:37]
	v_mfma_f32_16x16x32_bf16 v[22:25], v[152:155], v[192:195], v[22:25]
	v_mfma_f32_16x16x32_bf16 v[18:21], v[160:163], v[192:195], v[18:21]
	v_mfma_f32_16x16x32_bf16 v[62:65], v[156:159], v[172:175], v[62:65]
	v_mfma_f32_16x16x32_bf16 v[58:61], v[164:167], v[172:175], v[58:61]
	v_mfma_f32_16x16x32_bf16 v[54:57], v[156:159], v[180:183], v[54:57]
	v_mfma_f32_16x16x32_bf16 v[50:53], v[164:167], v[180:183], v[50:53]
	v_mfma_f32_16x16x32_bf16 v[38:41], v[156:159], v[188:191], v[38:41]
	v_mfma_f32_16x16x32_bf16 v[34:37], v[164:167], v[188:191], v[34:37]
	v_mfma_f32_16x16x32_bf16 v[22:25], v[156:159], v[196:199], v[22:25]
	v_mfma_f32_16x16x32_bf16 v[18:21], v[164:167], v[196:199], v[18:21]
	s_setprio 0
	s_barrier
	s_add_u32 s30, s30, 0x80080
	s_addc_u32 s31, s31, 0
	s_add_i32 s34, s34, s37
	s_mov_b32 m0, s34
	s_nop 0
	global_load_lds_dwordx4 v134, s[30:31]
	s_add_i32 m0, s34, 0x2000
	s_nop 0
	global_load_lds_dwordx4 v130, s[30:31]
	s_waitcnt vmcnt(6)
	s_barrier
	s_setprio 1
	v_mfma_f32_16x16x32_bf16 v[46:49], v[200:203], v[168:171], v[46:49]
	v_mfma_f32_16x16x32_bf16 v[42:45], v[210:213], v[168:171], v[42:45]
	v_mfma_f32_16x16x32_bf16 v[30:33], v[200:203], v[176:179], v[30:33]
	v_mfma_f32_16x16x32_bf16 v[26:29], v[210:213], v[176:179], v[26:29]
	v_mfma_f32_16x16x32_bf16 v[14:17], v[200:203], v[184:187], v[14:17]
	v_mfma_f32_16x16x32_bf16 v[10:13], v[210:213], v[184:187], v[10:13]
	v_mfma_f32_16x16x32_bf16 v[6:9], v[200:203], v[192:195], v[6:9]
	v_mfma_f32_16x16x32_bf16 v[2:5], v[210:213], v[192:195], v[2:5]
	v_mfma_f32_16x16x32_bf16 v[46:49], v[206:209], v[172:175], v[46:49]
	v_mfma_f32_16x16x32_bf16 v[42:45], v[214:217], v[172:175], v[42:45]
	v_mfma_f32_16x16x32_bf16 v[30:33], v[206:209], v[180:183], v[30:33]
	v_mfma_f32_16x16x32_bf16 v[26:29], v[214:217], v[180:183], v[26:29]
	v_mfma_f32_16x16x32_bf16 v[14:17], v[206:209], v[188:191], v[14:17]
	v_mfma_f32_16x16x32_bf16 v[10:13], v[214:217], v[188:191], v[10:13]
	v_mfma_f32_16x16x32_bf16 v[6:9], v[206:209], v[196:199], v[6:9]
	v_mfma_f32_16x16x32_bf16 v[2:5], v[214:217], v[196:199], v[2:5]
	s_setprio 0
	s_add_i32 s60, s60, 2
	s_add_u32 s28, s28, 0x100
	s_addc_u32 s29, s29, 0
	s_add_u32 s56, s56, 0x100
	s_addc_u32 s57, s57, 0
	s_cmp_gt_u32 s60, 29
	s_barrier
	s_cbranch_scc0 .LBB0_620
	v_lshl_add_u32 v152, s16, 8, v1
	v_lshl_or_b32 v154, s53, 8, v147
	v_ashrrev_i32_e32 v153, 31, v152
	v_ashrrev_i32_e32 v155, 31, v154
	v_lshlrev_b64 v[156:157], 12, v[152:153]
	v_lshl_add_u64 v[156:157], s[96:97], 0, v[156:157]
	v_lshlrev_b64 v[154:155], 1, v[154:155]
	v_lshl_add_u64 v[156:157], v[156:157], 0, v[154:155]
	v_cvt_pk_bf16_f32 v62, v62, v63
	v_cvt_pk_bf16_f32 v63, v64, v65
	v_cvt_pk_bf16_f32 v64, v58, v59
	v_add_co_u32_e32 v58, vcc, s49, v156
	v_cvt_pk_bf16_f32 v70, v70, v71
	v_cvt_pk_bf16_f32 v71, v72, v73
	v_cvt_pk_bf16_f32 v72, v66, v67
	v_lshl_add_u64 v[66:67], v[156:157], 0, s[6:7]
	v_addc_co_u32_e32 v59, vcc, 0, v157, vcc
	v_cvt_pk_bf16_f32 v46, v46, v47
	v_cvt_pk_bf16_f32 v47, v48, v49
	v_cvt_pk_bf16_f32 v48, v42, v43
	v_cvt_pk_bf16_f32 v49, v44, v45
	v_cvt_pk_bf16_f32 v110, v110, v111
	v_cvt_pk_bf16_f32 v111, v112, v113
	v_cvt_pk_bf16_f32 v112, v106, v107
	v_or_b32_e32 v106, 16, v152
	global_store_dwordx4 v[66:67], v[46:49], off offset:256
	v_ashrrev_i32_e32 v107, 31, v106
	v_cvt_pk_bf16_f32 v94, v94, v95
	v_add_co_u32_e32 v48, vcc, s50, v156
	v_cvt_pk_bf16_f32 v95, v96, v97
	v_cvt_pk_bf16_f32 v96, v90, v91
	v_or_b32_e32 v90, 32, v152
	v_lshl_add_u64 v[46:47], v[156:157], 0, s[10:11]
	v_addc_co_u32_e32 v49, vcc, 0, v157, vcc
	v_cvt_pk_bf16_f32 v30, v30, v31
	v_cvt_pk_bf16_f32 v31, v32, v33
	v_cvt_pk_bf16_f32 v32, v26, v27
	v_cvt_pk_bf16_f32 v33, v28, v29
	v_lshlrev_b64 v[106:107], 12, v[106:107]
	v_ashrrev_i32_e32 v91, 31, v90
	v_cvt_pk_bf16_f32 v78, v78, v79
	v_cvt_pk_bf16_f32 v79, v80, v81
	v_cvt_pk_bf16_f32 v80, v74, v75
	v_or_b32_e32 v74, 48, v152
	global_store_dwordx4 v[46:47], v[30:33], off offset:256
	v_cvt_pk_bf16_f32 v113, v108, v109
	v_lshl_add_u64 v[106:107], s[96:97], 0, v[106:107]
	v_add_co_u32_e32 v32, vcc, s51, v156
	v_lshlrev_b64 v[90:91], 12, v[90:91]
	v_ashrrev_i32_e32 v75, 31, v74
	v_lshl_add_u64 v[30:31], v[156:157], 0, s[12:13]
	v_addc_co_u32_e32 v33, vcc, 0, v157, vcc
	v_cvt_pk_bf16_f32 v14, v14, v15
	v_cvt_pk_bf16_f32 v15, v16, v17
	v_cvt_pk_bf16_f32 v16, v10, v11
	v_cvt_pk_bf16_f32 v17, v12, v13
	global_store_dwordx4 v[156:157], v[110:113], off offset:256
	v_cvt_pk_bf16_f32 v97, v92, v93
	v_lshl_add_u64 v[90:91], s[96:97], 0, v[90:91]
	v_lshl_add_u64 v[110:111], v[106:107], 0, v[154:155]
	v_lshlrev_b64 v[74:75], 12, v[74:75]
	global_store_dwordx4 v[30:31], v[14:17], off offset:256
	global_store_dwordx4 v[110:111], v[94:97], off offset:256
	v_cvt_pk_bf16_f32 v81, v76, v77
	v_add_co_u32_e32 v16, vcc, s52, v156
	v_lshl_add_u64 v[94:95], v[90:91], 0, v[154:155]
	v_lshl_add_u64 v[74:75], s[96:97], 0, v[74:75]
	v_addc_co_u32_e32 v17, vcc, 0, v157, vcc
	v_cvt_pk_bf16_f32 v126, v126, v127
	v_cvt_pk_bf16_f32 v127, v128, v129
	v_cvt_pk_bf16_f32 v128, v122, v123
	v_cvt_pk_bf16_f32 v129, v124, v125
	v_cvt_pk_bf16_f32 v106, v118, v119
	v_cvt_pk_bf16_f32 v107, v120, v121
	v_cvt_pk_bf16_f32 v108, v114, v115
	v_cvt_pk_bf16_f32 v109, v116, v117
	v_cvt_pk_bf16_f32 v90, v102, v103
	v_cvt_pk_bf16_f32 v91, v104, v105
	v_cvt_pk_bf16_f32 v92, v98, v99
	v_cvt_pk_bf16_f32 v93, v100, v101
	global_store_dwordx4 v[94:95], v[78:81], off offset:256
	v_cvt_pk_bf16_f32 v76, v82, v83
	v_cvt_pk_bf16_f32 v77, v84, v85
	v_lshl_add_u64 v[78:79], v[74:75], 0, v[154:155]
	v_cvt_pk_bf16_f32 v74, v86, v87
	v_cvt_pk_bf16_f32 v75, v88, v89
	v_cvt_pk_bf16_f32 v73, v68, v69
	v_cvt_pk_bf16_f32 v65, v60, v61
	v_cvt_pk_bf16_f32 v42, v54, v55
	v_cvt_pk_bf16_f32 v43, v56, v57
	v_cvt_pk_bf16_f32 v44, v50, v51
	v_cvt_pk_bf16_f32 v45, v52, v53
	v_cvt_pk_bf16_f32 v26, v38, v39
	v_cvt_pk_bf16_f32 v27, v40, v41
	v_cvt_pk_bf16_f32 v28, v34, v35
	v_cvt_pk_bf16_f32 v29, v36, v37
	v_lshl_add_u64 v[14:15], v[156:157], 0, s[14:15]
	v_cvt_pk_bf16_f32 v10, v22, v23
	v_cvt_pk_bf16_f32 v11, v24, v25
	v_cvt_pk_bf16_f32 v12, v18, v19
	v_cvt_pk_bf16_f32 v13, v20, v21
	v_cvt_pk_bf16_f32 v6, v6, v7
	v_cvt_pk_bf16_f32 v7, v8, v9
	v_cvt_pk_bf16_f32 v8, v2, v3
	v_cvt_pk_bf16_f32 v9, v4, v5
	s_and_b64 vcc, exec, s[0:1]
	s_mov_b32 s53, s18
	s_mov_b32 s16, s20
	s_mov_b64 s[30:31], s[26:27]
	s_mov_b64 s[28:29], s[22:23]
	global_store_dwordx4 v[156:157], v[126:129], off
	global_store_dwordx4 v[110:111], v[106:109], off
	global_store_dwordx4 v[94:95], v[90:93], off
	global_store_dwordx4 v[78:79], v[74:77], off
	global_store_dwordx4 v[78:79], v[70:73], off offset:256
	global_store_dwordx4 v[58:59], v[62:65], off
	global_store_dwordx4 v[48:49], v[42:45], off
	global_store_dwordx4 v[32:33], v[26:29], off
	global_store_dwordx4 v[16:17], v[10:13], off
	global_store_dwordx4 v[14:15], v[6:9], off offset:256
	s_cbranch_vccz .LBB0_617
	s_waitcnt vmcnt(0)
	s_cmpk_gt_u32 s2, 0xff
	s_cbranch_scc1 .LBB0_624
	s_barrier

.LBB0_1369:
	ds_read_b128 v[152:155], v149
	ds_read_b128 v[156:159], v246
	ds_read_b128 v[160:163], v149 offset:2048
	ds_read_b128 v[164:167], v246 offset:2048
	s_add_u32 s28, s26, 0xfff80080
	s_addc_u32 s29, s27, -1
	s_cmp_eq_u32 s54, 28
	s_cselect_b32 s31, s21, s29
	s_cselect_b32 s30, s50, s28
	s_cselect_b32 s29, s19, s53
	s_cselect_b32 s28, s51, s52
	s_add_i32 m0, s17, 0xc000
	ds_read_b128 v[168:171], v150
	ds_read_b128 v[172:175], v245
	ds_read_b128 v[176:179], v150 offset:2048
	ds_read_b128 v[180:183], v245 offset:2048
	ds_read_b128 v[184:187], v150 offset:4096
	ds_read_b128 v[190:193], v245 offset:4096
	ds_read_b128 v[194:197], v150 offset:6144
	ds_read_b128 v[198:201], v245 offset:6144
	global_load_lds_dwordx4 v138, s[26:27]
	s_add_i32 m0, s17, 0xe000
	s_nop 0
	global_load_lds_dwordx4 v140, s[26:27]
	s_waitcnt lgkmcnt(8)
	s_barrier
	s_waitcnt lgkmcnt(0)
	s_setprio 1
	s_waitcnt lgkmcnt(0)
	v_mfma_f32_16x16x32_bf16 v[126:129], v[152:155], v[168:171], v[126:129]
	v_mfma_f32_16x16x32_bf16 v[122:125], v[160:163], v[168:171], v[122:125]
	v_mfma_f32_16x16x32_bf16 v[118:121], v[152:155], v[176:179], v[118:121]
	v_mfma_f32_16x16x32_bf16 v[114:117], v[160:163], v[176:179], v[114:117]
	v_mfma_f32_16x16x32_bf16 v[102:105], v[152:155], v[184:187], v[102:105]
	v_mfma_f32_16x16x32_bf16 v[98:101], v[160:163], v[184:187], v[98:101]
	v_mfma_f32_16x16x32_bf16 v[86:89], v[152:155], v[194:197], v[86:89]
	v_mfma_f32_16x16x32_bf16 v[82:85], v[160:163], v[194:197], v[82:85]
	v_mfma_f32_16x16x32_bf16 v[126:129], v[156:159], v[172:175], v[126:129]
	v_mfma_f32_16x16x32_bf16 v[122:125], v[164:167], v[172:175], v[122:125]
	v_mfma_f32_16x16x32_bf16 v[118:121], v[156:159], v[180:183], v[118:121]
	v_mfma_f32_16x16x32_bf16 v[114:117], v[164:167], v[180:183], v[114:117]
	v_mfma_f32_16x16x32_bf16 v[102:105], v[156:159], v[190:193], v[102:105]
	v_mfma_f32_16x16x32_bf16 v[98:101], v[164:167], v[190:193], v[98:101]
	v_mfma_f32_16x16x32_bf16 v[86:89], v[156:159], v[198:201], v[86:89]
	v_mfma_f32_16x16x32_bf16 v[82:85], v[164:167], v[198:201], v[82:85]
	s_setprio 0
	s_barrier
	s_add_i32 s55, s43, s35
	s_add_u32 s66, s28, 0x80
	s_addc_u32 s67, s29, 0
	s_mov_b32 m0, s55
	ds_read_b128 v[214:217], v151
	ds_read_b128 v[218:221], v247
	ds_read_b128 v[222:225], v151 offset:2048
	ds_read_b128 v[226:229], v247 offset:2048
	global_load_lds_dwordx4 v132, s[28:29]
	s_add_i32 m0, s55, 0x2000
	s_nop 0
	global_load_lds_dwordx4 v136, s[28:29]
	s_barrier
	s_waitcnt lgkmcnt(0)
	s_setprio 1
	s_waitcnt lgkmcnt(0)
	v_mfma_f32_16x16x32_bf16 v[110:113], v[214:217], v[168:171], v[110:113]
	v_mfma_f32_16x16x32_bf16 v[106:109], v[222:225], v[168:171], v[106:109]
	v_mfma_f32_16x16x32_bf16 v[94:97], v[214:217], v[176:179], v[94:97]
	v_mfma_f32_16x16x32_bf16 v[90:93], v[222:225], v[176:179], v[90:93]
	v_mfma_f32_16x16x32_bf16 v[78:81], v[214:217], v[184:187], v[78:81]
	v_mfma_f32_16x16x32_bf16 v[74:77], v[222:225], v[184:187], v[74:77]
	v_mfma_f32_16x16x32_bf16 v[70:73], v[214:217], v[194:197], v[70:73]
	v_mfma_f32_16x16x32_bf16 v[66:69], v[222:225], v[194:197], v[66:69]
	v_mfma_f32_16x16x32_bf16 v[110:113], v[218:221], v[172:175], v[110:113]
	v_mfma_f32_16x16x32_bf16 v[106:109], v[226:229], v[172:175], v[106:109]
	v_mfma_f32_16x16x32_bf16 v[94:97], v[218:221], v[180:183], v[94:97]
	v_mfma_f32_16x16x32_bf16 v[90:93], v[226:229], v[180:183], v[90:93]
	v_mfma_f32_16x16x32_bf16 v[78:81], v[218:221], v[190:193], v[78:81]
	v_mfma_f32_16x16x32_bf16 v[74:77], v[226:229], v[190:193], v[74:77]
	v_mfma_f32_16x16x32_bf16 v[70:73], v[218:221], v[198:201], v[70:73]
	v_mfma_f32_16x16x32_bf16 v[66:69], v[226:229], v[198:201], v[66:69]
	s_setprio 0
	s_mov_b32 m0, s17
	s_add_u32 s68, s30, 0x80
	s_addc_u32 s69, s31, 0
	s_barrier
	ds_read_b128 v[168:171], v150 offset:16384
	ds_read_b128 v[172:175], v245 offset:16384
	ds_read_b128 v[176:179], v150 offset:18432
	ds_read_b128 v[180:183], v245 offset:18432
	ds_read_b128 v[184:187], v150 offset:20480
	ds_read_b128 v[190:193], v245 offset:20480
	ds_read_b128 v[194:197], v150 offset:22528
	ds_read_b128 v[198:201], v245 offset:22528
	global_load_lds_dwordx4 v130, s[30:31]
	s_mov_b32 m0, s36
	s_nop 0
	global_load_lds_dwordx4 v134, s[30:31]
	s_barrier
	s_waitcnt lgkmcnt(0)
	s_setprio 1
	s_waitcnt lgkmcnt(0)
	v_mfma_f32_16x16x32_bf16 v[62:65], v[152:155], v[168:171], v[62:65]
	v_mfma_f32_16x16x32_bf16 v[58:61], v[160:163], v[168:171], v[58:61]
	v_mfma_f32_16x16x32_bf16 v[54:57], v[152:155], v[176:179], v[54:57]
	v_mfma_f32_16x16x32_bf16 v[50:53], v[160:163], v[176:179], v[50:53]
	v_mfma_f32_16x16x32_bf16 v[38:41], v[152:155], v[184:187], v[38:41]
	v_mfma_f32_16x16x32_bf16 v[34:37], v[160:163], v[184:187], v[34:37]
	v_mfma_f32_16x16x32_bf16 v[22:25], v[152:155], v[194:197], v[22:25]
	v_mfma_f32_16x16x32_bf16 v[18:21], v[160:163], v[194:197], v[18:21]
	v_mfma_f32_16x16x32_bf16 v[62:65], v[156:159], v[172:175], v[62:65]
	v_mfma_f32_16x16x32_bf16 v[58:61], v[164:167], v[172:175], v[58:61]
	v_mfma_f32_16x16x32_bf16 v[54:57], v[156:159], v[180:183], v[54:57]
	v_mfma_f32_16x16x32_bf16 v[50:53], v[164:167], v[180:183], v[50:53]
	v_mfma_f32_16x16x32_bf16 v[38:41], v[156:159], v[190:193], v[38:41]
	v_mfma_f32_16x16x32_bf16 v[34:37], v[164:167], v[190:193], v[34:37]
	v_mfma_f32_16x16x32_bf16 v[22:25], v[156:159], v[198:201], v[22:25]
	v_mfma_f32_16x16x32_bf16 v[18:21], v[164:167], v[198:201], v[18:21]
	s_setprio 0
	s_barrier
	s_add_u32 s56, s28, 0x80000
	s_addc_u32 s57, s29, 0
	s_add_i32 s55, s44, s35
	s_mov_b32 m0, s55
	s_nop 0
	global_load_lds_dwordx4 v132, s[56:57]
	s_add_i32 m0, s55, 0x2000
	s_nop 0
	global_load_lds_dwordx4 v136, s[56:57]
	s_waitcnt vmcnt(6)
	s_barrier
	s_setprio 1
	v_mfma_f32_16x16x32_bf16 v[46:49], v[214:217], v[168:171], v[46:49]
	v_mfma_f32_16x16x32_bf16 v[42:45], v[222:225], v[168:171], v[42:45]
	v_mfma_f32_16x16x32_bf16 v[30:33], v[214:217], v[176:179], v[30:33]
	v_mfma_f32_16x16x32_bf16 v[26:29], v[222:225], v[176:179], v[26:29]
	v_mfma_f32_16x16x32_bf16 v[14:17], v[214:217], v[184:187], v[14:17]
	v_mfma_f32_16x16x32_bf16 v[10:13], v[222:225], v[184:187], v[10:13]
	v_mfma_f32_16x16x32_bf16 v[6:9], v[214:217], v[194:197], v[6:9]
	v_mfma_f32_16x16x32_bf16 v[2:5], v[222:225], v[194:197], v[2:5]
	v_mfma_f32_16x16x32_bf16 v[46:49], v[218:221], v[172:175], v[46:49]
	v_mfma_f32_16x16x32_bf16 v[42:45], v[226:229], v[172:175], v[42:45]
	v_mfma_f32_16x16x32_bf16 v[30:33], v[218:221], v[180:183], v[30:33]
	v_mfma_f32_16x16x32_bf16 v[26:29], v[226:229], v[180:183], v[26:29]
	v_mfma_f32_16x16x32_bf16 v[14:17], v[218:221], v[190:193], v[14:17]
	v_mfma_f32_16x16x32_bf16 v[10:13], v[226:229], v[190:193], v[10:13]
	v_mfma_f32_16x16x32_bf16 v[6:9], v[218:221], v[198:201], v[6:9]
	v_mfma_f32_16x16x32_bf16 v[2:5], v[226:229], v[198:201], v[2:5]
	s_setprio 0
	s_add_i32 s55, 0, 0x18000
	v_add_u32_e32 v164, s55, v147
	v_xor_b32_e32 v248, 64, v164
	s_barrier
	ds_read_b128 v[152:155], v164
	ds_read_b128 v[156:159], v248
	ds_read_b128 v[160:163], v164 offset:2048
	ds_read_b128 v[164:167], v248 offset:2048
	s_add_u32 s30, s30, 0x80000
	s_addc_u32 s31, s31, 0
	s_mov_b32 m0, s37
	ds_read_b128 v[168:171], v150 offset:32768
	ds_read_b128 v[172:175], v245 offset:32768
	ds_read_b128 v[176:179], v150 offset:34816
	ds_read_b128 v[180:183], v245 offset:34816
	ds_read_b128 v[184:187], v150 offset:36864
	ds_read_b128 v[190:193], v245 offset:36864
	ds_read_b128 v[194:197], v150 offset:38912
	ds_read_b128 v[198:201], v245 offset:38912
	global_load_lds_dwordx4 v130, s[30:31]
	s_mov_b32 m0, s38
	s_nop 0
	global_load_lds_dwordx4 v134, s[30:31]
	s_waitcnt lgkmcnt(8)
	s_barrier
	s_waitcnt lgkmcnt(0)
	s_setprio 1
	s_waitcnt lgkmcnt(0)
	v_mfma_f32_16x16x32_bf16 v[126:129], v[152:155], v[168:171], v[126:129]
	v_mfma_f32_16x16x32_bf16 v[122:125], v[160:163], v[168:171], v[122:125]
	v_mfma_f32_16x16x32_bf16 v[118:121], v[152:155], v[176:179], v[118:121]
	v_mfma_f32_16x16x32_bf16 v[114:117], v[160:163], v[176:179], v[114:117]
	v_mfma_f32_16x16x32_bf16 v[102:105], v[152:155], v[184:187], v[102:105]
	v_mfma_f32_16x16x32_bf16 v[98:101], v[160:163], v[184:187], v[98:101]
	v_mfma_f32_16x16x32_bf16 v[86:89], v[152:155], v[194:197], v[86:89]
	v_mfma_f32_16x16x32_bf16 v[82:85], v[160:163], v[194:197], v[82:85]
	v_mfma_f32_16x16x32_bf16 v[126:129], v[156:159], v[172:175], v[126:129]
	v_mfma_f32_16x16x32_bf16 v[122:125], v[164:167], v[172:175], v[122:125]
	v_mfma_f32_16x16x32_bf16 v[118:121], v[156:159], v[180:183], v[118:121]
	v_mfma_f32_16x16x32_bf16 v[114:117], v[164:167], v[180:183], v[114:117]
	v_mfma_f32_16x16x32_bf16 v[102:105], v[156:159], v[190:193], v[102:105]
	v_mfma_f32_16x16x32_bf16 v[98:101], v[164:167], v[190:193], v[98:101]
	v_mfma_f32_16x16x32_bf16 v[86:89], v[156:159], v[198:201], v[86:89]
	v_mfma_f32_16x16x32_bf16 v[82:85], v[164:167], v[198:201], v[82:85]
	s_setprio 0
	s_barrier
	s_add_i32 s30, 0, 0x1c000
	s_add_i32 s31, s55, s35
	v_add_u32_e32 v213, s30, v147
	v_xor_b32_e32 v249, 64, v213
	s_mov_b32 m0, s31
	ds_read_b128 v[214:217], v213
	ds_read_b128 v[218:221], v249
	ds_read_b128 v[222:225], v213 offset:2048
	ds_read_b128 v[226:229], v249 offset:2048
	global_load_lds_dwordx4 v132, s[66:67]
	s_add_i32 m0, s31, 0x2000
	s_nop 0
	global_load_lds_dwordx4 v136, s[66:67]
	s_barrier
	s_waitcnt lgkmcnt(0)
	s_setprio 1
	s_waitcnt lgkmcnt(0)
	v_mfma_f32_16x16x32_bf16 v[110:113], v[214:217], v[168:171], v[110:113]
	v_mfma_f32_16x16x32_bf16 v[106:109], v[222:225], v[168:171], v[106:109]
	v_mfma_f32_16x16x32_bf16 v[94:97], v[214:217], v[176:179], v[94:97]
	v_mfma_f32_16x16x32_bf16 v[90:93], v[222:225], v[176:179], v[90:93]
	v_mfma_f32_16x16x32_bf16 v[78:81], v[214:217], v[184:187], v[78:81]
	v_mfma_f32_16x16x32_bf16 v[74:77], v[222:225], v[184:187], v[74:77]
	v_mfma_f32_16x16x32_bf16 v[70:73], v[214:217], v[194:197], v[70:73]
	v_mfma_f32_16x16x32_bf16 v[66:69], v[222:225], v[194:197], v[66:69]
	v_mfma_f32_16x16x32_bf16 v[110:113], v[218:221], v[172:175], v[110:113]
	v_mfma_f32_16x16x32_bf16 v[106:109], v[226:229], v[172:175], v[106:109]
	v_mfma_f32_16x16x32_bf16 v[94:97], v[218:221], v[180:183], v[94:97]
	v_mfma_f32_16x16x32_bf16 v[90:93], v[226:229], v[180:183], v[90:93]
	v_mfma_f32_16x16x32_bf16 v[78:81], v[218:221], v[190:193], v[78:81]
	v_mfma_f32_16x16x32_bf16 v[74:77], v[226:229], v[190:193], v[74:77]
	v_mfma_f32_16x16x32_bf16 v[70:73], v[218:221], v[198:201], v[70:73]
	v_mfma_f32_16x16x32_bf16 v[66:69], v[226:229], v[198:201], v[66:69]
	s_setprio 0
	s_mov_b32 m0, s40
	s_barrier
	ds_read_b128 v[168:171], v150 offset:49152
	ds_read_b128 v[172:175], v245 offset:49152
	ds_read_b128 v[176:179], v150 offset:51200
	ds_read_b128 v[180:183], v245 offset:51200
	ds_read_b128 v[184:187], v150 offset:53248
	ds_read_b128 v[190:193], v245 offset:53248
	ds_read_b128 v[194:197], v150 offset:55296
	ds_read_b128 v[198:201], v245 offset:55296
	global_load_lds_dwordx4 v130, s[68:69]
	s_mov_b32 m0, s41
	s_nop 0
	global_load_lds_dwordx4 v134, s[68:69]
	s_barrier
	s_waitcnt lgkmcnt(0)
	s_setprio 1
	s_waitcnt lgkmcnt(0)
	v_mfma_f32_16x16x32_bf16 v[62:65], v[152:155], v[168:171], v[62:65]
	v_mfma_f32_16x16x32_bf16 v[58:61], v[160:163], v[168:171], v[58:61]
	v_mfma_f32_16x16x32_bf16 v[54:57], v[152:155], v[176:179], v[54:57]
	v_mfma_f32_16x16x32_bf16 v[50:53], v[160:163], v[176:179], v[50:53]
	v_mfma_f32_16x16x32_bf16 v[38:41], v[152:155], v[184:187], v[38:41]
	v_mfma_f32_16x16x32_bf16 v[34:37], v[160:163], v[184:187], v[34:37]
	v_mfma_f32_16x16x32_bf16 v[22:25], v[152:155], v[194:197], v[22:25]
	v_mfma_f32_16x16x32_bf16 v[18:21], v[160:163], v[194:197], v[18:21]
	v_mfma_f32_16x16x32_bf16 v[62:65], v[156:159], v[172:175], v[62:65]
	v_mfma_f32_16x16x32_bf16 v[58:61], v[164:167], v[172:175], v[58:61]
	v_mfma_f32_16x16x32_bf16 v[54:57], v[156:159], v[180:183], v[54:57]
	v_mfma_f32_16x16x32_bf16 v[50:53], v[164:167], v[180:183], v[50:53]
	v_mfma_f32_16x16x32_bf16 v[38:41], v[156:159], v[190:193], v[38:41]
	v_mfma_f32_16x16x32_bf16 v[34:37], v[164:167], v[190:193], v[34:37]
	v_mfma_f32_16x16x32_bf16 v[22:25], v[156:159], v[198:201], v[22:25]
	v_mfma_f32_16x16x32_bf16 v[18:21], v[164:167], v[198:201], v[18:21]
	s_setprio 0
	s_barrier
	s_add_u32 s28, s28, 0x80080
	s_addc_u32 s29, s29, 0
	s_add_i32 s30, s30, s35
	s_mov_b32 m0, s30
	s_nop 0
	global_load_lds_dwordx4 v132, s[28:29]
	s_add_i32 m0, s30, 0x2000
	s_nop 0
	global_load_lds_dwordx4 v136, s[28:29]
	s_waitcnt vmcnt(6)
	s_barrier
	s_setprio 1
	v_mfma_f32_16x16x32_bf16 v[46:49], v[214:217], v[168:171], v[46:49]
	v_mfma_f32_16x16x32_bf16 v[42:45], v[222:225], v[168:171], v[42:45]
	v_mfma_f32_16x16x32_bf16 v[30:33], v[214:217], v[176:179], v[30:33]
	v_mfma_f32_16x16x32_bf16 v[26:29], v[222:225], v[176:179], v[26:29]
	v_mfma_f32_16x16x32_bf16 v[14:17], v[214:217], v[184:187], v[14:17]
	v_mfma_f32_16x16x32_bf16 v[10:13], v[222:225], v[184:187], v[10:13]
	v_mfma_f32_16x16x32_bf16 v[6:9], v[214:217], v[194:197], v[6:9]
	v_mfma_f32_16x16x32_bf16 v[2:5], v[222:225], v[194:197], v[2:5]
	v_mfma_f32_16x16x32_bf16 v[46:49], v[218:221], v[172:175], v[46:49]
	v_mfma_f32_16x16x32_bf16 v[42:45], v[226:229], v[172:175], v[42:45]
	v_mfma_f32_16x16x32_bf16 v[30:33], v[218:221], v[180:183], v[30:33]
	v_mfma_f32_16x16x32_bf16 v[26:29], v[226:229], v[180:183], v[26:29]
	v_mfma_f32_16x16x32_bf16 v[14:17], v[218:221], v[190:193], v[14:17]
	v_mfma_f32_16x16x32_bf16 v[10:13], v[226:229], v[190:193], v[10:13]
	v_mfma_f32_16x16x32_bf16 v[6:9], v[218:221], v[198:201], v[6:9]
	v_mfma_f32_16x16x32_bf16 v[2:5], v[226:229], v[198:201], v[2:5]
	s_setprio 0
	s_add_i32 s54, s54, 2
	s_add_u32 s26, s26, 0x100
	s_addc_u32 s27, s27, 0
	s_add_u32 s52, s52, 0x100
	s_addc_u32 s53, s53, 0
	s_cmp_gt_u32 s54, 29
	s_barrier
	s_cbranch_scc0 .LBB0_1369
	v_lshl_add_u32 v152, s16, 8, v146
	v_lshl_or_b32 v154, s49, 8, v148
	v_ashrrev_i32_e32 v153, 31, v152
	v_ashrrev_i32_e32 v155, 31, v154
	v_lshlrev_b64 v[156:157], 12, v[152:153]
	v_lshl_add_u64 v[156:157], s[96:97], 0, v[156:157]
	v_lshlrev_b64 v[154:155], 1, v[154:155]
	v_lshl_add_u64 v[156:157], v[156:157], 0, v[154:155]
	v_cvt_pk_bf16_f32 v62, v62, v63
	v_cvt_pk_bf16_f32 v63, v64, v65
	v_cvt_pk_bf16_f32 v64, v58, v59
	v_add_co_u32_e32 v58, vcc, s45, v156
	v_cvt_pk_bf16_f32 v70, v70, v71
	v_cvt_pk_bf16_f32 v71, v72, v73
	v_cvt_pk_bf16_f32 v72, v66, v67
	v_lshl_add_u64 v[66:67], v[156:157], 0, s[6:7]
	v_addc_co_u32_e32 v59, vcc, 0, v157, vcc
	v_cvt_pk_bf16_f32 v46, v46, v47
	v_cvt_pk_bf16_f32 v47, v48, v49
	v_cvt_pk_bf16_f32 v48, v42, v43
	v_cvt_pk_bf16_f32 v49, v44, v45
	v_cvt_pk_bf16_f32 v110, v110, v111
	v_cvt_pk_bf16_f32 v111, v112, v113
	v_cvt_pk_bf16_f32 v112, v106, v107
	v_or_b32_e32 v106, 16, v152
	global_store_dwordx4 v[66:67], v[46:49], off offset:256
	v_ashrrev_i32_e32 v107, 31, v106
	v_cvt_pk_bf16_f32 v94, v94, v95
	v_add_co_u32_e32 v48, vcc, s46, v156
	v_cvt_pk_bf16_f32 v95, v96, v97
	v_cvt_pk_bf16_f32 v96, v90, v91
	v_or_b32_e32 v90, 32, v152
	v_lshl_add_u64 v[46:47], v[156:157], 0, s[10:11]
	v_addc_co_u32_e32 v49, vcc, 0, v157, vcc
	v_cvt_pk_bf16_f32 v30, v30, v31
	v_cvt_pk_bf16_f32 v31, v32, v33
	v_cvt_pk_bf16_f32 v32, v26, v27
	v_cvt_pk_bf16_f32 v33, v28, v29
	v_lshlrev_b64 v[106:107], 12, v[106:107]
	v_ashrrev_i32_e32 v91, 31, v90
	v_cvt_pk_bf16_f32 v78, v78, v79
	v_cvt_pk_bf16_f32 v79, v80, v81
	v_cvt_pk_bf16_f32 v80, v74, v75
	v_or_b32_e32 v74, 48, v152
	global_store_dwordx4 v[46:47], v[30:33], off offset:256
	v_cvt_pk_bf16_f32 v113, v108, v109
	v_lshl_add_u64 v[106:107], s[96:97], 0, v[106:107]
	v_add_co_u32_e32 v32, vcc, s47, v156
	v_lshlrev_b64 v[90:91], 12, v[90:91]
	v_ashrrev_i32_e32 v75, 31, v74
	v_lshl_add_u64 v[30:31], v[156:157], 0, s[12:13]
	v_addc_co_u32_e32 v33, vcc, 0, v157, vcc
	v_cvt_pk_bf16_f32 v14, v14, v15
	v_cvt_pk_bf16_f32 v15, v16, v17
	v_cvt_pk_bf16_f32 v16, v10, v11
	v_cvt_pk_bf16_f32 v17, v12, v13
	global_store_dwordx4 v[156:157], v[110:113], off offset:256
	v_cvt_pk_bf16_f32 v97, v92, v93
	v_lshl_add_u64 v[90:91], s[96:97], 0, v[90:91]
	v_lshl_add_u64 v[110:111], v[106:107], 0, v[154:155]
	v_lshlrev_b64 v[74:75], 12, v[74:75]
	global_store_dwordx4 v[30:31], v[14:17], off offset:256
	global_store_dwordx4 v[110:111], v[94:97], off offset:256
	v_cvt_pk_bf16_f32 v81, v76, v77
	v_add_co_u32_e32 v16, vcc, s48, v156
	v_lshl_add_u64 v[94:95], v[90:91], 0, v[154:155]
	v_lshl_add_u64 v[74:75], s[96:97], 0, v[74:75]
	v_addc_co_u32_e32 v17, vcc, 0, v157, vcc
	v_cvt_pk_bf16_f32 v126, v126, v127
	v_cvt_pk_bf16_f32 v127, v128, v129
	v_cvt_pk_bf16_f32 v128, v122, v123
	v_cvt_pk_bf16_f32 v129, v124, v125
	v_cvt_pk_bf16_f32 v106, v118, v119
	v_cvt_pk_bf16_f32 v107, v120, v121
	v_cvt_pk_bf16_f32 v108, v114, v115
	v_cvt_pk_bf16_f32 v109, v116, v117
	v_cvt_pk_bf16_f32 v90, v102, v103
	v_cvt_pk_bf16_f32 v91, v104, v105
	v_cvt_pk_bf16_f32 v92, v98, v99
	v_cvt_pk_bf16_f32 v93, v100, v101
	global_store_dwordx4 v[94:95], v[78:81], off offset:256
	v_cvt_pk_bf16_f32 v76, v82, v83
	v_cvt_pk_bf16_f32 v77, v84, v85
	v_lshl_add_u64 v[78:79], v[74:75], 0, v[154:155]
	v_cvt_pk_bf16_f32 v74, v86, v87
	v_cvt_pk_bf16_f32 v75, v88, v89
	v_cvt_pk_bf16_f32 v73, v68, v69
	v_cvt_pk_bf16_f32 v65, v60, v61
	v_cvt_pk_bf16_f32 v42, v54, v55
	v_cvt_pk_bf16_f32 v43, v56, v57
	v_cvt_pk_bf16_f32 v44, v50, v51
	v_cvt_pk_bf16_f32 v45, v52, v53
	v_cvt_pk_bf16_f32 v26, v38, v39
	v_cvt_pk_bf16_f32 v27, v40, v41
	v_cvt_pk_bf16_f32 v28, v34, v35
	v_cvt_pk_bf16_f32 v29, v36, v37
	v_lshl_add_u64 v[14:15], v[156:157], 0, s[14:15]
	v_cvt_pk_bf16_f32 v10, v22, v23
	v_cvt_pk_bf16_f32 v11, v24, v25
	v_cvt_pk_bf16_f32 v12, v18, v19
	v_cvt_pk_bf16_f32 v13, v20, v21
	v_cvt_pk_bf16_f32 v6, v6, v7
	v_cvt_pk_bf16_f32 v7, v8, v9
	v_cvt_pk_bf16_f32 v8, v2, v3
	v_cvt_pk_bf16_f32 v9, v4, v5
	s_and_b64 vcc, exec, s[0:1]
	s_mov_b32 s49, s18
	s_mov_b32 s16, s20
	s_mov_b64 s[28:29], s[24:25]
	s_mov_b64 s[26:27], s[22:23]
	global_store_dwordx4 v[156:157], v[126:129], off
	global_store_dwordx4 v[110:111], v[106:109], off
	global_store_dwordx4 v[94:95], v[90:93], off
	global_store_dwordx4 v[78:79], v[74:77], off
	global_store_dwordx4 v[78:79], v[70:73], off offset:256
	global_store_dwordx4 v[58:59], v[62:65], off
	global_store_dwordx4 v[48:49], v[42:45], off
	global_store_dwordx4 v[32:33], v[26:29], off
	global_store_dwordx4 v[16:17], v[10:13], off
	global_store_dwordx4 v[14:15], v[6:9], off offset:256
	s_cbranch_vccz .LBB0_1362
	s_waitcnt vmcnt(0)
	s_cmpk_gt_u32 s2, 0xff
	s_cbranch_scc1 .LBB0_1373
	s_barrier
